# attn loop2 (F copy): counted vmcnt(7..4) for the K/V prefetch consumed in the first half so the previous step's A stores stay in flight
# speedup vs baseline: 1.0096x; 1.0096x over previous
.Ll1_cont:
	ds_bpermute_b32 v2, v69, v84
	ds_bpermute_b32 v5, v69, v83
	v_max_f32_e32 v4, v84, v84
	v_max_f32_e32 v7, v83, v83
	ds_bpermute_b32 v3, v69, v63
	s_waitcnt lgkmcnt(2)
	v_max_f32_e32 v6, v2, v2
	v_max_f32_e32 v4, v4, v6
	v_sub_f32_e32 v6, v84, v4
	v_exp_f32_e32 v9, v6
	s_waitcnt lgkmcnt(1)
	v_max_f32_e32 v6, v5, v5
	v_sub_f32_e32 v2, v2, v4
	v_max_f32_e32 v6, v7, v6
	v_exp_f32_e32 v11, v2
	ds_bpermute_b32 v2, v69, v62
	v_sub_f32_e32 v5, v5, v6
	v_sub_f32_e32 v7, v83, v6
	v_exp_f32_e32 v10, v5
	v_exp_f32_e32 v8, v7
	v_cmp_gt_u32_e32 vcc, 32, v98
	s_waitcnt lgkmcnt(0)
	v_pk_mul_f32 v[2:3], v[10:11], v[2:3]
	s_nop 0
	v_pk_fma_f32 v[8:9], v[62:63], v[8:9], v[2:3]
	v_lshlrev_b32_e32 v2, 7, v184
	v_or3_b32 v10, v183, v2, v1
	s_and_saveexec_b64 s[0:1], vcc
	v_lshl_add_u32 v2, v10, 4, 0
	v_add_u32_e32 v2, 0x21000, v2
	v_mov_b32_e32 v5, v9
	v_mov_b32_e32 v7, v8
	ds_write_b128 v2, v[4:7]
	s_or_b64 exec, exec, s[0:1]
	s_lshl_b32 s12, s21, 7
	s_mov_b32 s3, 0
	v_or_b32_e32 v2, s12, v82
	s_lshl_b32 s13, s21, 11
	s_add_i32 s23, 0, 0x12000
	v_lshlrev_b32_e32 v2, 12, v2
	v_mov_b32_e32 v3, 0
	s_add_i32 s13, s13, s16
	s_lshl_b64 s[0:1], s[2:3], 13
	v_lshl_add_u64 v[12:13], s[14:15], 0, v[2:3]
	v_mov_b32_e32 v69, v3
	s_add_u32 s0, s10, s0
	v_lshl_add_u64 v[172:173], v[12:13], 0, v[68:69]
	s_addc_u32 s1, s11, s1
	s_lshl_b32 s10, s22, 7
	s_mov_b32 s11, s3
	s_waitcnt vmcnt(1)
	v_lshl_add_u64 v[36:37], v[172:173], 0, s[10:11]
	s_mov_b32 s10, 0x40000
	v_add_co_u32_e32 v38, vcc, s10, v36
	s_waitcnt lgkmcnt(0)
	s_barrier
	global_load_dwordx4 v[12:15], v[58:59], off
	global_load_dwordx4 v[16:19], v[70:71], off
	v_addc_co_u32_e32 v39, vcc, 0, v37, vcc
	global_load_dwordx4 v[20:23], v[56:57], off
	global_load_dwordx4 v[24:27], v[66:67], off
	global_load_dwordx4 v[28:31], v[36:37], off
	global_load_dwordx4 v[32:35], v[38:39], off
	v_add_f32_e32 v2, v78, v80
	s_movk_i32 s11, 0x1200
	v_add_f32_e32 v5, v79, v81
	s_mov_b32 s14, 0x3fb8aa3b
	v_lshlrev_b32_e32 v10, 4, v10
	v_mov_b32_e32 v36, s23
	v_mul_f32_e32 v37, 0x3fb8aa3b, v2
	v_mul_f32_e32 v38, 0x3fb8aa3b, v5
	v_xor_b32_e32 v10, 0x800, v10
	v_mad_u32_u24 v40, v55, s11, v36
	v_fma_f32 v36, v2, s14, -v37
	v_rndne_f32_e32 v39, v37
	v_fma_f32 v41, v5, s14, -v38
	s_waitcnt vmcnt(6)
	v_rndne_f32_e32 v42, v38
	v_add_u32_e32 v10, 0, v10
	v_fmac_f32_e32 v36, 0x32a5705f, v2
	v_sub_f32_e32 v37, v37, v39
	v_fmac_f32_e32 v41, 0x32a5705f, v5
	v_sub_f32_e32 v38, v38, v42
	v_add_u32_e32 v10, 0x21000, v10
	v_add_f32_e32 v44, v37, v36
	global_load_dwordx4 v[146:149], v[60:61], off
	global_load_dwordx4 v[150:153], v[64:65], off
	v_cvt_i32_f32_e32 v43, v39
	v_add_f32_e32 v41, v38, v41
	ds_read_b128 v[36:39], v10
	v_exp_f32_e32 v10, v44
	v_cvt_i32_f32_e32 v42, v42
	v_exp_f32_e32 v41, v41
	s_mov_b32 s21, 0xc2ce8ed0
	s_lshl_b32 s11, s20, 6
	s_add_i32 s14, s11, 64
	v_ldexp_f32 v10, v10, v43
	v_cmp_ngt_f32_e32 vcc, s21, v2
	s_mov_b32 s22, 0x42b17218
	s_and_b32 s14, s14, 0x7c0
	v_ldexp_f32 v41, v41, v42
	v_cndmask_b32_e32 v10, 0, v10, vcc
	v_cmp_ngt_f32_e32 vcc, s21, v5
	v_mov_b32_e32 v7, 0x7f800000
	v_max_f32_e32 v11, v4, v4
	s_mov_b32 s15, s3
	s_lshl_b32 s14, s14, 1
	s_waitcnt lgkmcnt(0)
	v_max_f32_e32 v42, v36, v36
	v_cndmask_b32_e32 v41, 0, v41, vcc
	v_cmp_nlt_f32_e32 vcc, s22, v2
	v_max_f32_e32 v187, v11, v42
	v_mov_b32_e32 v55, v3
	v_cndmask_b32_e32 v2, v7, v10, vcc
	v_cmp_nlt_f32_e32 vcc, s22, v5
	v_lshl_add_u64 v[10:11], v[172:173], 0, s[14:15]
	v_lshl_add_u64 v[178:179], s[0:1], 0, v[54:55]
	v_cndmask_b32_e32 v5, v7, v41, vcc
	v_sub_f32_e32 v2, v2, v5
	v_add_f32_e32 v41, 0x3e4ccccd, v2
	v_sub_f32_e32 v2, v4, v187
	v_max_f32_e32 v4, v6, v6
	s_and_b32 s1, s2, 7
	s_mulk_i32 s1, 0x280
	s_mulk_i32 s19, 0x140
	s_add_i32 s0, s20, 2
	s_waitcnt vmcnt(7)
	ds_write_b128 v185, v[12:15]
	s_waitcnt vmcnt(6)
	ds_write_b128 v185, v[16:19] offset:9216
	s_waitcnt vmcnt(5)
	ds_write_b128 v185, v[20:23] offset:18432
	s_waitcnt vmcnt(4)
	ds_write_b128 v185, v[24:27] offset:27648
	s_waitcnt vmcnt(3)
	ds_write_b128 v185, v[28:31] offset:36864
	s_waitcnt vmcnt(2)
	ds_write_b128 v185, v[32:35] offset:46080
	v_add_co_u32_e32 v12, vcc, s10, v10
	v_exp_f32_e32 v23, v2
	s_nop 0
	v_addc_co_u32_e32 v13, vcc, 0, v11, vcc
	global_load_dwordx4 v[154:157], v[10:11], off
	global_load_dwordx4 v[158:161], v[12:13], off
	s_waitcnt lgkmcnt(0)
	s_barrier
	ds_read_b128 v[10:13], v186
	v_sub_f32_e32 v2, v36, v187
	v_exp_f32_e32 v25, v2
	v_max_f32_e32 v2, v38, v38
	v_max_f32_e32 v188, v4, v2
	v_sub_f32_e32 v2, v6, v188
	v_exp_f32_e32 v22, v2
	v_sub_f32_e32 v2, v38, v188
	v_exp_f32_e32 v24, v2
	ds_read_b128 v[14:17], v186 offset:9216
	ds_read_b128 v[18:21], v186 offset:32
	s_waitcnt lgkmcnt(2)
	v_mfma_f32_32x32x16_f16 v[66:81], v[10:13], v[114:117], 0
	v_mov_b32_e32 v36, v39
	v_mul_f32_e64 v10, v36, v24
	v_mul_f32_e64 v11, v37, v25
	ds_read_b128 v[4:7], v186 offset:9248
	s_add_i32 s1, s1, s19
	s_mov_b32 s14, 0x30000
	s_mov_b32 s15, 0x80000
	s_mov_b32 s19, 0
	s_waitcnt lgkmcnt(2)
	v_mfma_f32_32x32x16_f16 v[82:97], v[14:17], v[130:133], 0
	v_fma_f32 v16, v8, v22, v10
	v_fma_f32 v17, v9, v23, v11
	v_log_f32_e32 v238, v17
	s_nop 0
	v_add_f32_e32 v187, v187, v238
	v_sub_f32_e32 v240, 0, v187
	v_sub_f32_e32 v241, 0, v187
	v_sub_f32_e32 v242, 0, v187
	v_sub_f32_e32 v243, 0, v187
	v_sub_f32_e32 v244, 0, v187
	v_sub_f32_e32 v245, 0, v187
	v_sub_f32_e32 v246, 0, v187
	v_sub_f32_e32 v247, 0, v187
	v_sub_f32_e32 v248, 0, v187
	v_sub_f32_e32 v249, 0, v187
	v_sub_f32_e32 v250, 0, v187
	v_sub_f32_e32 v251, 0, v187
	v_sub_f32_e32 v252, 0, v187
	v_sub_f32_e32 v253, 0, v187
	v_sub_f32_e32 v254, 0, v187
	v_sub_f32_e32 v255, 0, v187
	v_lshrrev_b32_e32 v22, 3, v98
	v_or3_b32 v2, s13, v183, v22
	v_lshlrev_b64 v[8:9], 13, v[2:3]
	v_lshl_add_u64 v[8:9], s[4:5], 0, v[8:9]
	v_lshlrev_b32_e32 v2, 2, v101
	v_lshl_add_u64 v[8:9], v[8:9], 0, v[2:3]
	v_and_b32_e32 v2, 0x70, v54
	v_lshl_add_u64 v[174:175], v[8:9], 0, v[2:3]
	ds_read_b128 v[8:11], v186 offset:64
	s_waitcnt lgkmcnt(2)
	v_mfma_f32_32x32x16_f16 v[66:81], v[18:21], v[118:121], v[66:81]
	v_div_scale_f32 v18, s[4:5], v16, v16, -v41
	v_rcp_f32_e32 v19, v18
	v_div_scale_f32 v20, vcc, -v41, v16, -v41
	s_mov_b32 s13, 0x20000
	v_mov_b32_e32 v24, v3
	s_waitcnt lgkmcnt(1)
	v_mfma_f32_32x32x16_f16 v[82:97], v[4:7], v[134:137], v[82:97]
	v_fma_f32 v4, -v18, v19, 1.0
	v_fmac_f32_e32 v19, v4, v19
	v_mul_f32_e32 v21, v20, v19
	ds_read_b128 v[4:7], v186 offset:9280
	ds_read_b128 v[12:15], v186 offset:96
	v_mov_b32_e32 v25, v3
	v_mov_b32_e32 v26, v3
	v_mov_b32_e32 v27, v3
	s_waitcnt lgkmcnt(2)
	v_mfma_f32_32x32x16_f16 v[66:81], v[8:11], v[122:125], v[66:81]
	v_fma_f32 v8, -v18, v21, v20
	v_fmac_f32_e32 v21, v8, v19
	v_fma_f32 v18, -v18, v21, v20
	v_div_scale_f32 v20, s[4:5], v17, v17, 1.0
	v_rcp_f32_e32 v23, v20
	ds_read_b128 v[8:11], v186 offset:9312
	s_waitcnt lgkmcnt(2)
	v_mfma_f32_32x32x16_f16 v[82:97], v[4:7], v[138:141], v[82:97]
	v_div_fmas_f32 v4, v18, v19, v21
	v_div_fixup_f32 v176, v4, v16, -v41
	v_fma_f32 v4, -v20, v23, 1.0
	v_fmac_f32_e32 v23, v4, v23
	v_div_scale_f32 v4, vcc, 1.0, v17, 1.0
	v_mul_f32_e32 v5, v4, v23
	v_fma_f32 v6, -v20, v5, v4
	v_fmac_f32_e32 v5, v6, v23
	s_waitcnt lgkmcnt(1)
	v_mfma_f32_32x32x16_f16 v[66:81], v[12:15], v[126:129], v[66:81]
	v_fma_f32 v4, -v20, v5, v4
	v_div_fmas_f32 v4, v4, v23, v5
	v_div_fixup_f32 v177, v4, v17, 1.0
	v_mul_u32_u24_e32 v4, 0x90, v22
	v_add3_u32 v189, v40, v4, v2
	v_mul_u32_u24_e32 v2, 0x90, v1
	v_lshlrev_b32_e32 v4, 2, v99
	s_waitcnt lgkmcnt(0)
	v_mfma_f32_32x32x16_f16 v[82:97], v[8:11], v[142:145], v[82:97]
	v_add3_u32 v190, v40, v2, v4
	v_mul_u32_u24_e32 v2, 0x48, v1
	v_lshl_add_u32 v2, v2, 1, 0
	v_lshlrev_b32_e32 v4, 1, v101
	v_add3_u32 v191, v2, v4, v100
	s_mov_b32 s4, 0x3f800000
	s_mov_b32 s5, 0x10000
	v_mov_b32_e32 v2, v3
	v_mov_b32_e32 v4, v3
	v_mov_b32_e32 v5, v3
	v_mov_b32_e32 v6, v3
	v_mov_b32_e32 v7, v3
	v_mov_b32_e32 v8, v3
	v_mov_b32_e32 v9, v3
	v_mov_b32_e32 v10, v3
	v_mov_b32_e32 v11, v3
	v_mov_b32_e32 v12, v3
	v_mov_b32_e32 v13, v3
	v_mov_b32_e32 v14, v3
	v_mov_b32_e32 v15, v3
	v_mov_b32_e32 v16, v3
	v_mov_b32_e32 v17, v3
	v_mov_b32_e32 v18, v3
	v_mov_b32_e32 v19, v3
	v_mov_b32_e32 v20, v3
	v_mov_b32_e32 v21, v3
	v_mov_b32_e32 v22, v3
	v_mov_b32_e32 v23, v3
	v_mov_b32_e32 v28, v3
	v_mov_b32_e32 v29, v3
	v_mov_b32_e32 v30, v3
	v_mov_b32_e32 v31, v3
	v_mov_b32_e32 v32, v3
	v_mov_b32_e32 v33, v3
	v_mov_b32_e32 v34, v3
	v_mov_b32_e32 v35, v3
	v_mov_b32_e32 v36, v3
	v_mov_b32_e32 v37, v3
	v_mov_b32_e32 v38, v3
	v_mov_b32_e32 v39, v3
	v_mov_b32_e32 v40, v3
	v_mov_b32_e32 v41, v3
	v_mov_b32_e32 v42, v3
	v_mov_b32_e32 v43, v3
	v_mov_b32_e32 v44, v3
	v_mov_b32_e32 v45, v3
	v_mov_b32_e32 v46, v3
	v_mov_b32_e32 v47, v3
	v_mov_b32_e32 v48, v3
	v_mov_b32_e32 v49, v3
	v_mov_b32_e32 v50, v3
	v_mov_b32_e32 v51, v3
	v_mov_b32_e32 v52, v3
	v_mov_b32_e32 v53, v3
	v_mov_b32_e32 v54, v3
	v_mov_b32_e32 v56, v3
	v_mov_b32_e32 v57, v3
	v_mov_b32_e32 v58, v3
	v_mov_b32_e32 v59, v3
	v_mov_b32_e32 v60, v3
	v_mov_b32_e32 v61, v3
	v_mov_b32_e32 v62, v3
	v_mov_b32_e32 v63, v3
	v_mov_b32_e32 v64, v3
	v_mov_b32_e32 v65, v3
	v_add_u32_e32 v192, 0xd800, v191
	v_sub_f32_e32 v66, v66, v187
	v_sub_f32_e32 v67, v67, v187
	v_sub_f32_e32 v68, v68, v187
	v_sub_f32_e32 v69, v69, v187
	v_sub_f32_e32 v70, v70, v187
	v_sub_f32_e32 v71, v71, v187
	v_sub_f32_e32 v72, v72, v187
	v_sub_f32_e32 v73, v73, v187
	v_sub_f32_e32 v74, v74, v187
	v_sub_f32_e32 v75, v75, v187
	v_sub_f32_e32 v76, v76, v187
	v_sub_f32_e32 v77, v77, v187
	v_sub_f32_e32 v78, v78, v187
	v_sub_f32_e32 v79, v79, v187
	v_sub_f32_e32 v80, v80, v187
	v_sub_f32_e32 v81, v81, v187
	s_mov_b32 s27, 0x42c80000
	v_cmp_gt_f32_e64 vcc, |v188|, s27
	s_cbranch_vccnz .Ll2_gen
	v_sub_f32_e32 v238, 0, v188
	v_exp_f32_e32 v238, v238
	s_nop 0
	v_mul_f32_e32 v176, v176, v238
	s_waitcnt vmcnt(0)
	s_barrier
	s_branch .Ll2f_top

.Ll2f_top:
	ds_read_b128 v[98:101], v186 offset:18432
	ds_read_b128 v[162:165], v186 offset:18464
	ds_read_b128 v[194:197], v186 offset:27648
	ds_read_b128 v[198:201], v186 offset:27680
	ds_read_b128 v[202:205], v186 offset:18496
	ds_read_b128 v[206:209], v186 offset:18528
	ds_read_b128 v[210:213], v186 offset:27712
	ds_read_b128 v[166:169], v186 offset:27744
	s_nop 0
	v_exp_f32_e32 v215, v66
	v_exp_f32_e32 v217, v67
	v_exp_f32_e32 v219, v68
	v_exp_f32_e32 v221, v69
	v_exp_f32_e32 v223, v70
	v_exp_f32_e32 v71, v71
	v_exp_f32_e32 v225, v72
	v_exp_f32_e32 v227, v73
	v_exp_f32_e32 v229, v74
	v_exp_f32_e32 v231, v75
	s_waitcnt lgkmcnt(7)
	v_mfma_f32_32x32x16_f16 v[98:113], v[98:101], v[114:117], v[240:255]
	v_exp_f32_e32 v216, v82
	v_exp_f32_e32 v214, v83
	v_exp_f32_e32 v220, v84
	v_exp_f32_e32 v218, v85
	v_exp_f32_e32 v70, v86
	v_exp_f32_e32 v222, v87
	v_exp_f32_e32 v226, v88
	v_exp_f32_e32 v224, v89
	s_waitcnt lgkmcnt(6)
	v_mfma_f32_32x32x16_f16 v[98:113], v[162:165], v[118:121], v[98:113]
	v_exp_f32_e32 v233, v76
	v_exp_f32_e32 v235, v77
	v_exp_f32_e32 v230, v90
	v_exp_f32_e32 v228, v91
	v_exp_f32_e32 v234, v92
	v_exp_f32_e32 v232, v93
	v_exp_f32_e32 v237, v78
	v_exp_f32_e32 v236, v95
	s_waitcnt lgkmcnt(3)
	v_mfma_f32_32x32x16_f16 v[98:113], v[202:205], v[122:125], v[98:113]
	v_exp_f32_e32 v162, v94
	v_exp_f32_e32 v163, v79
	v_exp_f32_e32 v165, v80
	v_exp_f32_e32 v202, v96
	v_exp_f32_e32 v203, v81
	v_exp_f32_e32 v193, v97
	s_waitcnt lgkmcnt(2)
	v_mfma_f32_32x32x16_f16 v[98:113], v[206:209], v[126:129], v[98:113]
	s_waitcnt vmcnt(7)
	ds_write_b128 v185, v[146:149]
	s_waitcnt vmcnt(6)
	ds_write_b128 v185, v[150:153] offset:9216
	s_waitcnt vmcnt(5)
	ds_write_b128 v185, v[154:157] offset:55296
	s_waitcnt vmcnt(4)
	ds_write_b128 v185, v[158:161] offset:64512
	v_fma_f32 v150, v176, v216, v215
	v_fma_f32 v151, v176, v214, v217
	ds_read_b128 v[66:69], v189
	ds_read_b128 v[88:91], v189 offset:1152
	v_fma_f32 v152, v176, v220, v219
	v_fma_f32 v153, v176, v218, v221
	ds_read_b128 v[92:95], v189 offset:2304
	ds_read_b128 v[146:149], v189 offset:3456
	v_fma_f32 v154, v176, v70, v223
	v_fma_f32 v155, v176, v222, v71
	ds_write_b128 v190, v[150:153]
	v_fma_f32 v156, v176, v226, v225
	v_fma_f32 v157, v176, v224, v227
	ds_write_b128 v190, v[154:157] offset:16
	v_fma_f32 v158, v176, v230, v229
	v_fma_f32 v159, v176, v228, v231
	v_cvt_pk_f16_f32 v157, v156, v157
	v_fma_f32 v160, v176, v234, v233
	v_fma_f32 v161, v176, v232, v235
	ds_write_b128 v190, v[158:161] offset:64
	v_fma_f32 v162, v176, v162, v237
	v_fma_f32 v163, v176, v236, v163
	v_cvt_pk_f16_f32 v156, v154, v155
	v_fma_f32 v164, v176, v202, v165
	v_fma_f32 v165, v176, v193, v203
	ds_write_b128 v190, v[162:165] offset:80
	v_cvt_pk_f16_f32 v155, v152, v153
	v_cvt_pk_f16_f32 v154, v150, v151
	ds_read_b128 v[150:153], v191 offset:36864
	s_cmp_eq_u32 s19, 0
	s_cselect_b64 vcc, -1, 0
	s_add_i32 s20, s16, s1
	v_mfma_f32_32x32x16_f16 v[72:87], v[194:197], v[130:133], 0
	ds_read_b128 v[194:197], v191 offset:36896
	s_add_i32 s2, s20, 0x7c0
	s_and_b32 s2, s2, 0x7c0
	s_lshl_b32 s2, s2, 2
	v_lshl_add_u64 v[70:71], v[174:175], 0, s[2:3]
	v_cndmask_b32_e32 v71, v71, v179, vcc
	v_cndmask_b32_e32 v70, v70, v178, vcc
	s_waitcnt lgkmcnt(1)
	v_mfma_f32_32x32x16_f16 v[50:65], v[154:157], v[150:153], v[50:65]
	ds_read_b128 v[150:153], v191 offset:41472
	global_store_dwordx4 v[70:71], v[66:69], off nt
	ds_read_b128 v[66:69], v191 offset:41504
	v_cvt_pk_f16_f32 v165, v164, v165
	v_cvt_pk_f16_f32 v164, v162, v163
	v_cvt_pk_f16_f32 v163, v160, v161
	v_cvt_pk_f16_f32 v162, v158, v159
	s_waitcnt lgkmcnt(1)
	v_mfma_f32_32x32x16_f16 v[34:49], v[154:157], v[150:153], v[34:49]
	v_add_co_u32_e32 v96, vcc, s5, v70
	s_min_u32 s2, s19, 28
	s_nop 0
	v_addc_co_u32_e32 v97, vcc, 0, v71, vcc
	global_store_dwordx4 v[96:97], v[88:91], off nt
	s_add_i32 s21, s17, s2
	s_waitcnt lgkmcnt(0)
	v_mfma_f32_32x32x16_f16 v[34:49], v[162:165], v[66:69], v[34:49]
	ds_read_b128 v[66:69], v191 offset:46080
	v_add_co_u32_e32 v88, vcc, s13, v70
	s_lshl_b32 s2, s21, 13
	s_nop 0
	v_addc_co_u32_e32 v89, vcc, 0, v71, vcc
	global_store_dwordx4 v[88:89], v[92:95], off nt
	ds_read_b128 v[88:91], v191 offset:46112
	s_waitcnt lgkmcnt(1)
	v_mfma_f32_32x32x16_f16 v[18:33], v[154:157], v[66:69], v[18:33]
	v_add_co_u32_e32 v70, vcc, s14, v70
	s_and_b32 s2, s2, 0x3e000
	s_nop 0
	v_addc_co_u32_e32 v71, vcc, 0, v71, vcc
	v_lshl_add_u64 v[66:67], v[170:171], 0, s[2:3]
	v_add_co_u32_e32 v68, vcc, s15, v66
	global_store_dwordx4 v[70:71], v[146:149], off nt
	s_nop 0
	v_addc_co_u32_e32 v69, vcc, 0, v67, vcc
	s_waitcnt lgkmcnt(0)
	v_mfma_f32_32x32x16_f16 v[18:33], v[162:165], v[88:91], v[18:33]
	global_load_dwordx4 v[88:91], v[66:67], off
	global_load_dwordx4 v[92:95], v[68:69], off
	ds_read_b128 v[66:69], v191 offset:50688
	ds_read_b128 v[146:149], v191 offset:50720
	s_min_u32 s2, s19, 29
	s_add_i32 s2, s0, s2
	s_lshl_b32 s2, s2, 7
	s_and_b32 s2, s2, 0xf80
	s_waitcnt lgkmcnt(1)
	v_mfma_f32_32x32x16_f16 v[2:17], v[154:157], v[66:69], v[2:17]
	v_lshl_add_u64 v[66:67], v[172:173], 0, s[2:3]
	v_add_co_u32_e32 v68, vcc, s10, v66
	s_nop 0
	v_addc_co_u32_e32 v69, vcc, 0, v67, vcc
	global_load_dwordx4 v[150:153], v[66:67], off
	global_load_dwordx4 v[154:157], v[68:69], off
	v_mfma_f32_32x32x16_f16 v[72:87], v[198:201], v[134:137], v[72:87]
	v_exp_f32_e32 v97, v98
	s_waitcnt lgkmcnt(0)
	s_barrier
	v_mfma_f32_32x32x16_f16 v[72:87], v[210:213], v[138:141], v[72:87]
	v_mfma_f32_32x32x16_f16 v[72:87], v[166:169], v[142:145], v[72:87]
	v_mfma_f32_32x32x16_f16 v[50:65], v[162:165], v[194:197], v[50:65]
	s_nop 0
	ds_read_b128 v[66:69], v186
	ds_read_b128 v[158:161], v186 offset:32
	ds_read_b128 v[194:197], v186 offset:9216
	ds_read_b128 v[198:201], v186 offset:9248
	ds_read_b128 v[202:205], v186 offset:64
	ds_read_b128 v[206:209], v186 offset:96
	v_exp_f32_e32 v167, v99
	v_exp_f32_e32 v99, v100
	v_exp_f32_e32 v169, v101
	v_exp_f32_e32 v101, v102
	v_mfma_f32_32x32x16_f16 v[2:17], v[162:165], v[146:149], v[2:17]
	ds_read_b128 v[146:149], v186 offset:9280
	ds_read_b128 v[162:165], v186 offset:9312
	v_exp_f32_e32 v211, v103
	v_exp_f32_e32 v103, v104
	v_exp_f32_e32 v213, v105
	v_exp_f32_e32 v105, v106
	v_exp_f32_e32 v215, v107
	v_exp_f32_e32 v107, v108
	v_exp_f32_e32 v217, v109
	v_exp_f32_e32 v166, v72
	v_exp_f32_e32 v96, v73
	v_exp_f32_e32 v168, v74
	v_exp_f32_e32 v98, v75
	v_exp_f32_e32 v210, v76
	v_exp_f32_e32 v100, v77
	v_exp_f32_e32 v212, v78
	v_exp_f32_e32 v102, v79
	v_exp_f32_e32 v214, v80
	v_exp_f32_e32 v104, v81
	s_waitcnt lgkmcnt(7)
	v_mfma_f32_32x32x16_f16 v[66:81], v[66:69], v[114:117], v[240:255]
	v_exp_f32_e32 v109, v110
	v_exp_f32_e32 v216, v82
	v_exp_f32_e32 v106, v83
	v_exp_f32_e32 v219, v111
	s_waitcnt lgkmcnt(6)
	v_mfma_f32_32x32x16_f16 v[66:81], v[158:161], v[118:121], v[66:81]
	v_exp_f32_e32 v218, v84
	v_exp_f32_e32 v108, v85
	v_exp_f32_e32 v111, v112
	v_exp_f32_e32 v110, v87
	s_waitcnt lgkmcnt(3)
	v_mfma_f32_32x32x16_f16 v[66:81], v[202:205], v[122:125], v[66:81]
	v_exp_f32_e32 v202, v86
	v_exp_f32_e32 v203, v113
	s_waitcnt lgkmcnt(2)
	v_mfma_f32_32x32x16_f16 v[66:81], v[206:209], v[126:129], v[66:81]
	s_waitcnt vmcnt(3)
	ds_write_b128 v185, v[88:91] offset:18432
	s_waitcnt vmcnt(2)
	ds_write_b128 v185, v[92:95] offset:27648
	s_waitcnt vmcnt(1)
	ds_write_b128 v185, v[150:153] offset:36864
	s_waitcnt vmcnt(0)
	ds_write_b128 v185, v[154:157] offset:46080
	v_fma_f32 v150, v176, v166, v97
	v_fma_f32 v151, v176, v96, v167
	v_mfma_f32_32x32x16_f16 v[82:97], v[194:197], v[130:133], 0
	v_fma_f32 v152, v176, v168, v99
	v_fma_f32 v153, v176, v98, v169
	v_fma_f32 v154, v176, v210, v101
	v_fma_f32 v155, v176, v100, v211
	v_fma_f32 v156, v176, v212, v103
	v_fma_f32 v157, v176, v102, v213
	v_fma_f32 v158, v176, v214, v105
	v_fma_f32 v159, v176, v104, v215
	v_fma_f32 v160, v176, v216, v107
	v_fma_f32 v161, v176, v106, v217
	v_fma_f32 v166, v176, v218, v109
	v_fma_f32 v167, v176, v108, v219
	v_fma_f32 v168, v176, v202, v111
	v_fma_f32 v169, v176, v110, v203
	ds_read_b128 v[98:101], v189
	ds_read_b128 v[102:105], v189 offset:1152
	ds_read_b128 v[106:109], v189 offset:2304
	ds_read_b128 v[110:113], v189 offset:3456
	ds_write_b128 v190, v[150:153]
	ds_write_b128 v190, v[154:157] offset:16
	ds_write_b128 v190, v[158:161] offset:64
	ds_write_b128 v190, v[166:169] offset:80
	v_cvt_pk_f16_f32 v157, v156, v157
	v_cvt_pk_f16_f32 v156, v154, v155
	v_cvt_pk_f16_f32 v155, v152, v153
	v_cvt_pk_f16_f32 v154, v150, v151
	ds_read_b128 v[150:153], v191 offset:55296
	ds_read_b128 v[194:197], v191 offset:55328
	v_mfma_f32_32x32x16_f16 v[82:97], v[198:201], v[134:137], v[82:97]
	s_and_b32 s2, s20, 0x7c0
	s_min_u32 s20, s19, 27
	s_lshl_b32 s2, s2, 2
	s_add_i32 s20, s18, s20
	v_lshl_add_u64 v[210:211], v[174:175], 0, s[2:3]
	s_lshl_b32 s2, s20, 13
	s_and_b32 s2, s2, 0x3e000
	s_waitcnt lgkmcnt(1)
	v_mfma_f32_32x32x16_f16 v[50:65], v[154:157], v[150:153], v[50:65]
	ds_read_b128 v[150:153], v191 offset:59904
	ds_read_b128 v[198:201], v191 offset:59936
	s_lshl_b32 s21, s21, 7
	v_cvt_pk_f16_f32 v169, v168, v169
	v_cvt_pk_f16_f32 v168, v166, v167
	v_cvt_pk_f16_f32 v166, v158, v159
	v_cvt_pk_f16_f32 v167, v160, v161
	s_addk_i32 s1, 0x80
	s_waitcnt lgkmcnt(1)
	v_mfma_f32_32x32x16_f16 v[34:49], v[154:157], v[150:153], v[34:49]
	ds_read_b128 v[150:153], v191 offset:64512
	ds_read_b128 v[202:205], v191 offset:64544
	s_waitcnt lgkmcnt(1)
	v_mfma_f32_32x32x16_f16 v[18:33], v[154:157], v[150:153], v[18:33]
	ds_read_b128 v[150:153], v192 offset:13824
	ds_read_b128 v[206:209], v192 offset:13856
	v_mfma_f32_32x32x16_f16 v[82:97], v[146:149], v[138:141], v[82:97]
	v_lshl_add_u64 v[146:147], v[170:171], 0, s[2:3]
	s_and_b32 s2, s21, 0xf80
	v_lshl_add_u64 v[158:159], v[172:173], 0, s[2:3]
	s_add_i32 s2, s19, 2
	s_cmp_lt_u32 s19, 30
	s_mov_b32 s19, s2
	s_waitcnt lgkmcnt(1)
	v_mfma_f32_32x32x16_f16 v[2:17], v[154:157], v[150:153], v[2:17]
	v_add_co_u32_e32 v150, vcc, s15, v146
	s_nop 1
	v_addc_co_u32_e32 v151, vcc, 0, v147, vcc
	global_load_dwordx4 v[146:149], v[146:147], off
	s_nop 0
	global_load_dwordx4 v[150:153], v[150:151], off
	s_nop 0
	global_load_dwordx4 v[154:157], v[158:159], off
	v_add_co_u32_e32 v158, vcc, s10, v158
	v_mfma_f32_32x32x16_f16 v[50:65], v[166:169], v[194:197], v[50:65]
	s_nop 0
	v_addc_co_u32_e32 v159, vcc, 0, v159, vcc
	global_load_dwordx4 v[158:161], v[158:159], off
	v_add_co_u32_e32 v194, vcc, s5, v210
	s_nop 1
	v_addc_co_u32_e32 v195, vcc, 0, v211, vcc
	v_mfma_f32_32x32x16_f16 v[34:49], v[166:169], v[198:201], v[34:49]
	v_add_co_u32_e32 v196, vcc, s13, v210
	s_nop 1
	v_addc_co_u32_e32 v197, vcc, 0, v211, vcc
	v_mfma_f32_32x32x16_f16 v[18:33], v[166:169], v[202:205], v[18:33]
	s_waitcnt lgkmcnt(0)
	v_mfma_f32_32x32x16_f16 v[2:17], v[166:169], v[206:209], v[2:17]
	v_add_co_u32_e32 v166, vcc, s14, v210
	s_nop 1
	v_addc_co_u32_e32 v167, vcc, 0, v211, vcc
	global_store_dwordx4 v[210:211], v[98:101], off nt
	global_store_dwordx4 v[194:195], v[102:105], off nt
	global_store_dwordx4 v[196:197], v[106:109], off nt
	global_store_dwordx4 v[166:167], v[110:113], off nt
	v_mfma_f32_32x32x16_f16 v[82:97], v[162:165], v[142:145], v[82:97]
	s_barrier
	s_cbranch_scc1 .Ll2f_top
